# nt11 + P0 wave specialization: waves 0-3 run their weight-fold item first, waves 4-7 last (fold overlaps HBM streaming)
# baseline (speedup 1.0000x reference)
; #define LAS __attribute__((address_space(3)))
; __global__ void __launch_bounds__(NWAVES * 64, 2) fwd(Args args) {
;     extern __shared__ __attribute__((aligned(16))) unsigned char lds[];
;     Frame F;
;     F.lds = (LAS unsigned char*)lds;
;     F.MISC = (volatile LAS unsigned*)(F.lds + MISC_OFF);
;     F.tid = threadIdx.x; F.lane = F.tid & 63; F.wave = __builtin_amdgcn_readfirstlane(F.tid >> 6);
;     F.G = gridDim.x; { const int bx = blockIdx.x; F.vcu = (F.G % 8 == 0) ? (bx % 8) * (F.G / 8) + bx / 8 : bx; }
_Z3fwd4Args:
	s_mov_b32 s98, 0
	s_load_dword s4, s[0:1], 0x88
	s_add_u32 s6, s0, 0x88
	s_addc_u32 s7, s1, 0
	v_readfirstlane_b32 s3, v0
	v_writelane_b32 v255, s6, 0
	s_nop 1
	v_writelane_b32 v255, s7, 1
	s_waitcnt lgkmcnt(0)
	v_writelane_b32 v255, s4, 2
	s_and_b32 s4, s4, 7
	s_cmp_eq_u32 s4, 0
	s_cselect_b64 s[8:9], -1, 0
	v_writelane_b32 v255, s8, 3
	s_mov_b32 s6, 0
	s_cmp_lg_u32 s4, 0
	v_writelane_b32 v255, s9, 4
	s_mov_b32 s4, s2
	s_cbranch_scc1 .LBB0_2
	s_load_dword s4, s[0:1], 0x88
	s_ashr_i32 s5, s2, 31
	s_lshr_b32 s5, s5, 29
	s_add_i32 s5, s2, s5
	s_and_b32 s7, s5, -8
	s_waitcnt lgkmcnt(0)
	s_ashr_i32 s4, s4, 3
	s_sub_i32 s7, s2, s7
	s_mul_i32 s4, s4, s7
	s_ashr_i32 s5, s5, 3
	s_add_i32 s4, s4, s5

; __device__ __forceinline__ void p0_prologue(Frame& F) {
;     ...
;     const int gw = F.vcu * NWAVES + F.wave, NGW = F.G * NWAVES;
;     bf16* WINT = (bf16*)(F.ws + WS_WINT); bf16* WCOT = (bf16*)(F.ws + WS_WCOT);
;     constexpr int I_1 = (DM / 64) * (INC / 32), I_2 = (CD / 64) * (DM / 32), I_3 = (AD / 64) * (DM / 32), I_4 = (DM / 64) * (DM / 32);
;     constexpr int NITEMS = I_1 + I_2 + I_3 + I_4;
;     struct TItem { const float* src; unsigned char* dst; int N, ldo, fp8; float sc; };
;     ...
;     auto decode = [&](int it) { TItem t; int r = it;
;         if (r < I_1) { const int kb = P0_KB(r, INC / 32), nb = P0_NB(r, INC / 32); t.src = F.in[I_WIN] + (size_t)(64 * kb) * INC + 32 * nb; t.N = INC;
;             if (nb < Z8_COL0 / 32) { t.fp8 = 0; t.ldo = 2 * LDP; t.dst = (unsigned char*)WINT + (size_t)(32 * nb) * (2 * LDP) + 2 * 64 * kb; t.sc = 1.f; }
;             else { t.fp8 = LOWP; t.ldo = 2 * LDP8; t.dst = (unsigned char*)(F.ws + WS_WIN8) + (size_t)(32 * nb - Z8_COL0) * (2 * LDP8) + 64 * kb; t.sc = WIN8_SCALE; }
;             return t; } r -= I_1;
;         if (r < I_2) { const int kb = P0_KB(r, DM / 32), nb = P0_NB(r, DM / 32); t.src = F.in[I_WCO] + (size_t)(64 * kb) * DM + 32 * nb; t.N = DM;
;             if (GEMM2_FUSED) { t.fp8 = 1; t.ldo = 2 * LDP8; t.dst = (unsigned char*)(F.ws + WS_WC) + (size_t)(32 * nb) * (2 * LDP8) + 64 * kb; t.sc = WCO8_SCALE; }
;             else if (CONVOUT_INT8 || CONVOUT_FP8) { t.fp8 = CONVOUT_FP8 ? 1 : 2; t.ldo = 2 * LDH8; t.dst = (unsigned char*)WCOT + (size_t)(32 * nb) * (2 * LDH8) + 64 * kb; t.sc = WCO8_SCALE; }
;             else { t.fp8 = 0; t.ldo = 2 * LDH; t.dst = (unsigned char*)WCOT + (size_t)(32 * nb) * (2 * LDH) + 2 * 64 * kb; t.sc = 1.f; }
;             return t; } r -= I_2;
;         if (r < I_3) { const int kb = P0_KB(r, DM / 32), nb = P0_NB(r, DM / 32); t.src = F.in[I_WAO] + (size_t)(64 * kb) * DM + 32 * nb; t.N = DM; t.fp8 = 1; t.sc = WAO8_SCALE;
;             if (GEMM2_FUSED) { t.ldo = 2 * LDP8; t.dst = (unsigned char*)(F.ws + WS_WC) + (size_t)(32 * nb) * (2 * LDP8) + 2048 + 64 * kb; }
;             else { t.ldo = 2 * LDH8; t.dst = (unsigned char*)(F.ws + WS_WAO8) + (size_t)(32 * nb) * (2 * LDH8) + 64 * kb; }
;             return t; } r -= I_3;
;         { const int kb = P0_KB(r, DM / 32), nb = P0_NB(r, DM / 32); t.src = F.in[I_WO] + (size_t)(64 * kb) * DM + 32 * nb; t.N = DM;
.LBB0_11:
	s_or_b64 exec, exec, s[4:5]
	s_load_dwordx2 s[4:5], s[0:1], 0x80
	s_lshr_b32 s0, s3, 6
	v_writelane_b32 v255, s0, 10
	v_and_b32_e32 v202, 63, v0
	s_waitcnt lgkmcnt(0)
	s_cmp_lt_i32 s4, 1
	s_cselect_b64 s[0:1], -1, 0
	v_writelane_b32 v255, s4, 11
	s_cmp_gt_i32 s5, 0
	s_nop 0
	v_writelane_b32 v255, s5, 12
	s_cselect_b64 s[4:5], -1, 0
	s_and_b64 s[4:5], s[0:1], s[4:5]
	s_andn2_b64 vcc, exec, s[4:5]
	s_cbranch_vccnz .LBB0_102
	s_lshl_b32 s0, s97, 3
	v_readlane_b32 s1, v255, 10
	s_add_i32 s6, s0, s1
	v_readlane_b32 s0, v255, 2
	s_lshl_b32 s33, s0, 3
	s_cmp_gt_u32 s1, 3
	s_cbranch_scc1 .Lp0_main
	s_mov_b32 s98, 1
	s_branch .LBB0_97
.Lp0_main:
	s_cmp_gt_i32 s6, 0xdfff
	s_cbranch_scc1 .LBB0_92
	s_add_u32 s7, s66, 0x200000
	s_addc_u32 s42, s67, 0
	s_cmp_gt_i32 s6, 0x9fff
	s_cbranch_scc0 .LBB0_18
	s_cmpk_gt_u32 s6, 0xafff
	s_cbranch_scc0 .LBB0_19
	s_lshl_b32 s0, s6, 4
	s_bfe_u32 s30, s3, 0x10006
	s_and_b32 s29, s0, 0xfe0
	s_cmpk_gt_u32 s6, 0xbfff
	s_mov_b32 s1, 0
	s_mul_i32 s28, s29, 0x1080
	s_cbranch_scc0 .LBB0_148
	s_add_i32 s0, s6, 0xffff4000
	s_lshr_b32 s0, s0, 7
	s_and_b32 s0, s0, 0x1fffffe
	s_or_b32 s0, s0, s30
	s_lshl_b32 s0, s0, 6
	s_lshl_b64 s[24:25], s[0:1], 14
	s_add_u32 s1, s22, s24
	s_addc_u32 s25, s23, s25
	s_lshl_b32 s24, s29, 2
	s_add_u32 s24, s1, s24
	s_addc_u32 s25, s25, 0
	s_add_u32 s1, s66, s28
	s_addc_u32 s26, s67, 0
	s_add_u32 s0, s1, s0
	s_addc_u32 s1, s26, 0
	s_add_u32 s0, s0, 0xa800000
	s_addc_u32 s1, s1, 0
	s_mov_b32 s70, 1
	s_cbranch_execz .LBB0_149
	s_mov_b32 s70, 2
	s_mov_b32 s41, 0x45000000
	s_cbranch_execz .LBB0_20
	s_branch .LBB0_21

; __device__ __forceinline__ void p0_prologue(Frame& F) {
;     ...
;     {
;         bf16* WF = (bf16*)(F.ws + WS_WPQF); const float* SK = F.in[I_SUBK]; const float* WQ = F.in[I_WPQ];
;         const int l15 = F.lane & 15, l4 = F.lane >> 4;
;         for (int task = gw; task < 2048; task += NGW) {
;             const int combo = task & 127, kr = task >> 7, hc = combo >> 3, kt = combo & 7, n0 = hc * 128 + kt * 16;
;             bf16x8 bfr[4];
; #pragma unroll
;             for (int ds = 0; ds < 4; ++ds) bfr[ds] = cvt8(SK + (size_t)(n0 + l15) * 128 + ds * 32 + 8 * l4);
.LBB0_97:
	s_cmp_eq_u32 s98, 2
	s_cbranch_scc1 .LBB0_102
	s_cmpk_gt_i32 s6, 0x7ff
	s_cbranch_scc1 .LBB0_102
	s_waitcnt vmcnt(7)
	v_lshrrev_b32_e32 v2, 4, v202
	v_readlane_b32 s1, v255, 10
	v_lshlrev_b32_e32 v114, 5, v2
	v_mov_b32_e32 v115, 0
	s_lshl_b32 s0, s97, 4
	s_lshl_b32 s1, s1, 1
	v_lshl_add_u64 v[116:117], s[56:57], 0, v[114:115]
	v_lshl_add_u64 v[118:119], s[54:55], 0, v[114:115]
	v_lshlrev_b32_e32 v114, 2, v2
	s_add_i32 s7, s0, s1
	v_readlane_b32 s0, v255, 2
	v_and_b32_e32 v1, 15, v0
	v_lshl_add_u64 v[120:121], s[66:67], 0, v[114:115]
	s_lshl_b32 s12, s0, 4
	s_mov_b32 s1, 0
	s_movk_i32 s13, 0x7fff
	s_mov_b32 s18, 0xffff0000
	s_movk_i32 s19, 0xff81
	s_mov_b32 s20, 0x40c0c00
	s_mov_b32 s21, 0xc900000
	v_mov_b32_e32 v123, 0x7f

; #define LAS __attribute__((address_space(3)))
; __device__ __forceinline__ void p0_prologue(Frame& F) {
;     LAS float* scr = (LAS float*)(F.lds + RING_OFF + F.wave * 16384);
;     const int gw = F.vcu * NWAVES + F.wave, NGW = F.G * NWAVES;
;     bf16* WINT = (bf16*)(F.ws + WS_WINT); bf16* WCOT = (bf16*)(F.ws + WS_WCOT);
; __global__ void __launch_bounds__(NWAVES * 64, 2) fwd(Args args) {
;     ...
;     F.ws = args.ws; F.out = args.out; F.ctl = (gu32*)(args.ws + WS_CTL);
; #pragma unroll
;     for (int i = 0; i < N_IN; ++i) F.in[i] = args.in[i];
.LBB0_102:
	s_cmp_eq_u32 s98, 1
	s_cbranch_scc0 .Lp0_end
	s_mov_b32 s98, 2
	v_readlane_b32 s6, v255, 0
	v_readlane_b32 s7, v255, 1
	s_sub_u32 s6, s6, 0x88
	s_subb_u32 s7, s7, 0
	s_load_dwordx16 s[8:23], s[6:7], 0x0
	s_waitcnt lgkmcnt(0)
	s_lshl_b32 s0, s97, 3
	v_readlane_b32 s1, v255, 10
	s_add_i32 s6, s0, s1
	s_branch .Lp0_main
